# grid-barrier seams: acquire-side buffer_inv sc1 issued once per workgroup at arrival (before the arrival atomic) instead of after the rendezvous on both the leader and the poller paths
# speedup vs baseline: 1.0085x; 1.0017x over previous
; __device__ __forceinline__ unsigned xb_ld(unsigned* p)              { return __hip_atomic_load(p, __ATOMIC_RELAXED, __HIP_MEMORY_SCOPE_AGENT); }
; __device__ __forceinline__ unsigned xb_add(unsigned* p, unsigned v) { return __hip_atomic_fetch_add(p, v, __ATOMIC_RELAXED, __HIP_MEMORY_SCOPE_AGENT); }
; #define XB_SPIN(cond, bar) do { unsigned _sp = 0; while (cond) { __builtin_amdgcn_s_sleep(1); \
;     if ((++_sp & 255u) == 0u) { if (xb_ld(&(bar)[XB_TMO])) break; if (_sp > XB_SPIN_CAP) { atomicAdd(&(bar)[XB_TMO], 1u); break; } } } } while (0)
; __device__ __forceinline__ void xcd_barrier(const XcdBarrier& b) {
;     ...
;         const unsigned old = xb_add(&bar[XB_XSUB(b.x)], 1u);
;         const unsigned gen = old / nloc;
;         if (old + 1u == (gen + 1u) * nloc) {
;             __builtin_amdgcn_fence(__ATOMIC_RELEASE, "agent");
;             asm volatile("s_waitcnt vmcnt(0)" ::: "memory");
;             const unsigned og = xb_add(&bar[XB_TOP], 1u);
;             const unsigned tg = og / nx;
;             if (og + 1u == (tg + 1u) * nx) xb_add(&bar[XB_TOPGEN], 1u);
;             else XB_SPIN(xb_ld(&bar[XB_TOPGEN]) == tg, bar);
;             __builtin_amdgcn_fence(__ATOMIC_ACQUIRE, "agent");
;             xb_add(&bar[XB_XGEN(b.x)], 1u);
;             asm volatile("s_waitcnt vmcnt(0)" ::: "memory");
;         } else {
;             XB_SPIN(xb_ld(&bar[XB_XGEN(b.x)]) == gen, bar);
;             __builtin_amdgcn_fence(__ATOMIC_ACQUIRE, "agent");
.LBB0_215:
	v_readlane_b32 s6, v252, 44
	s_lshl_b32 s6, s6, 2
	s_add_u32 s6, s4, s6
	s_addc_u32 s7, s5, 0
	v_mov_b32_e32 v1, 0x1000
	v_cvt_f32_u32_e32 v3, v4
	buffer_inv sc1
	global_atomic_add v5, v1, v181, s[6:7] offset:1024 sc0
	v_sub_u32_e32 v6, 0, v4
	v_rcp_iflag_f32_e32 v3, v3
	s_nop 0
	v_mul_f32_e32 v3, 0x4f7ffffe, v3
	v_cvt_u32_f32_e32 v3, v3
	v_mul_lo_u32 v6, v6, v3
	v_mul_hi_u32 v6, v3, v6
	v_add_u32_e32 v3, v3, v6
	s_waitcnt vmcnt(0)
	v_mul_hi_u32 v3, v5, v3
	v_mul_lo_u32 v6, v3, v4
	v_sub_u32_e32 v6, v5, v6
	v_add_u32_e32 v7, 1, v3
	v_cmp_ge_u32_e32 vcc, v6, v4
	v_add_u32_e32 v5, 1, v5
	s_nop 0
	v_cndmask_b32_e32 v3, v3, v7, vcc
	v_sub_u32_e32 v7, v6, v4
	v_cndmask_b32_e32 v6, v6, v7, vcc
	v_add_u32_e32 v7, 1, v3
	v_cmp_ge_u32_e32 vcc, v6, v4
	s_nop 1
	v_cndmask_b32_e32 v3, v3, v7, vcc
	v_mul_lo_u32 v6, v4, v3
	v_add_u32_e32 v4, v6, v4
	v_cmp_ne_u32_e32 vcc, v5, v4
	s_and_saveexec_b64 s[8:9], vcc
	s_xor_b64 s[8:9], exec, s[8:9]
	s_cbranch_execz .LBB0_229
	v_mov_b32_e32 v1, 0x2000
	s_waitcnt lgkmcnt(0)
	global_load_dword v2, v1, s[6:7] offset:1024 sc1
	s_add_u32 s14, s6, 0x2400
	s_addc_u32 s15, s7, 0
	s_waitcnt vmcnt(0)
	v_cmp_eq_u32_e32 vcc, v2, v3
	s_and_saveexec_b64 s[10:11], vcc
	s_cbranch_execz .LBB0_228
	s_mov_b32 s12, 1
	s_mov_b64 s[16:17], 0
	s_branch .LBB0_219

; __device__ __forceinline__ unsigned xb_ld(unsigned* p)              { return __hip_atomic_load(p, __ATOMIC_RELAXED, __HIP_MEMORY_SCOPE_AGENT); }
; #define XB_SPIN(cond, bar) do { unsigned _sp = 0; while (cond) { __builtin_amdgcn_s_sleep(1); \
;     if ((++_sp & 255u) == 0u) { if (xb_ld(&(bar)[XB_TMO])) break; if (_sp > XB_SPIN_CAP) { atomicAdd(&(bar)[XB_TMO], 1u); break; } } } } while (0)
; __device__ __forceinline__ void xcd_barrier(const XcdBarrier& b) {
;     ...
;             XB_SPIN(xb_ld(&bar[XB_XGEN(b.x)]) == gen, bar);
;             __builtin_amdgcn_fence(__ATOMIC_ACQUIRE, "agent");
;             asm volatile("s_waitcnt vmcnt(0)" ::: "memory");
.LBB0_228:
	s_or_b64 exec, exec, s[10:11]
	s_waitcnt vmcnt(0)
	s_waitcnt vmcnt(0)

; __device__ __forceinline__ unsigned xb_ld(unsigned* p)              { return __hip_atomic_load(p, __ATOMIC_RELAXED, __HIP_MEMORY_SCOPE_AGENT); }
; __device__ __forceinline__ unsigned xb_add(unsigned* p, unsigned v) { return __hip_atomic_fetch_add(p, v, __ATOMIC_RELAXED, __HIP_MEMORY_SCOPE_AGENT); }
; #define XB_SPIN(cond, bar) do { unsigned _sp = 0; while (cond) { __builtin_amdgcn_s_sleep(1); \
;     if ((++_sp & 255u) == 0u) { if (xb_ld(&(bar)[XB_TMO])) break; if (_sp > XB_SPIN_CAP) { atomicAdd(&(bar)[XB_TMO], 1u); break; } } } } while (0)
; __device__ __forceinline__ void xcd_barrier(const XcdBarrier& b) {
;     ...
;             else XB_SPIN(xb_ld(&bar[XB_TOPGEN]) == tg, bar);
;             __builtin_amdgcn_fence(__ATOMIC_ACQUIRE, "agent");
;             xb_add(&bar[XB_XGEN(b.x)], 1u);
;             asm volatile("s_waitcnt vmcnt(0)" ::: "memory");
.LBB0_246:
	s_or_b64 exec, exec, s[4:5]
	v_mov_b32_e32 v1, 0x2000
	s_waitcnt vmcnt(0)
	global_atomic_add v1, v181, s[6:7] offset:1024
	s_waitcnt vmcnt(0)

; __device__ __forceinline__ unsigned xb_ld(unsigned* p)              { return __hip_atomic_load(p, __ATOMIC_RELAXED, __HIP_MEMORY_SCOPE_AGENT); }
; __device__ __forceinline__ unsigned xb_add(unsigned* p, unsigned v) { return __hip_atomic_fetch_add(p, v, __ATOMIC_RELAXED, __HIP_MEMORY_SCOPE_AGENT); }
; #define XB_SPIN(cond, bar) do { unsigned _sp = 0; while (cond) { __builtin_amdgcn_s_sleep(1); \
;     if ((++_sp & 255u) == 0u) { if (xb_ld(&(bar)[XB_TMO])) break; if (_sp > XB_SPIN_CAP) { atomicAdd(&(bar)[XB_TMO], 1u); break; } } } } while (0)
; __device__ __forceinline__ void xcd_barrier(const XcdBarrier& b) {
;     ...
;         const unsigned old = xb_add(&bar[XB_XSUB(b.x)], 1u);
;         const unsigned gen = old / nloc;
;         if (old + 1u == (gen + 1u) * nloc) {
;             __builtin_amdgcn_fence(__ATOMIC_RELEASE, "agent");
;             asm volatile("s_waitcnt vmcnt(0)" ::: "memory");
;             const unsigned og = xb_add(&bar[XB_TOP], 1u);
;             const unsigned tg = og / nx;
;             if (og + 1u == (tg + 1u) * nx) xb_add(&bar[XB_TOPGEN], 1u);
;             else XB_SPIN(xb_ld(&bar[XB_TOPGEN]) == tg, bar);
.LBB0_340:
	v_readlane_b32 s6, v252, 44
	s_lshl_b32 s6, s6, 2
	s_add_u32 s6, s4, s6
	s_addc_u32 s7, s5, 0
	v_mov_b32_e32 v1, 0x1000
	v_cvt_f32_u32_e32 v3, v4
	buffer_inv sc1
	global_atomic_add v5, v1, v181, s[6:7] offset:1024 sc0
	v_sub_u32_e32 v6, 0, v4
	v_rcp_iflag_f32_e32 v3, v3
	s_nop 0
	v_mul_f32_e32 v3, 0x4f7ffffe, v3
	v_cvt_u32_f32_e32 v3, v3
	v_mul_lo_u32 v6, v6, v3
	v_mul_hi_u32 v6, v3, v6
	v_add_u32_e32 v3, v3, v6
	s_waitcnt vmcnt(0)
	v_mul_hi_u32 v3, v5, v3
	v_mul_lo_u32 v6, v3, v4
	v_sub_u32_e32 v6, v5, v6
	v_add_u32_e32 v7, 1, v3
	v_cmp_ge_u32_e32 vcc, v6, v4
	v_add_u32_e32 v5, 1, v5
	s_nop 0
	v_cndmask_b32_e32 v3, v3, v7, vcc
	v_sub_u32_e32 v7, v6, v4
	v_cndmask_b32_e32 v6, v6, v7, vcc
	v_add_u32_e32 v7, 1, v3
	v_cmp_ge_u32_e32 vcc, v6, v4
	s_nop 1
	v_cndmask_b32_e32 v3, v3, v7, vcc
	v_mul_lo_u32 v6, v4, v3
	v_add_u32_e32 v4, v6, v4
	v_cmp_ne_u32_e32 vcc, v5, v4
	s_and_saveexec_b64 s[8:9], vcc
	s_xor_b64 s[8:9], exec, s[8:9]
	s_cbranch_execz .LBB0_354
	v_mov_b32_e32 v1, 0x2000
	s_waitcnt lgkmcnt(0)
	global_load_dword v2, v1, s[6:7] offset:1024 sc1
	s_add_u32 s14, s6, 0x2400
	s_addc_u32 s15, s7, 0
	s_waitcnt vmcnt(0)
	v_cmp_eq_u32_e32 vcc, v2, v3
	s_and_saveexec_b64 s[10:11], vcc
	s_cbranch_execz .LBB0_353
	s_mov_b32 s26, 1
	s_mov_b64 s[16:17], 0
	s_branch .LBB0_344

; __device__ __forceinline__ unsigned xb_ld(unsigned* p)              { return __hip_atomic_load(p, __ATOMIC_RELAXED, __HIP_MEMORY_SCOPE_AGENT); }
; __device__ __forceinline__ unsigned xb_add(unsigned* p, unsigned v) { return __hip_atomic_fetch_add(p, v, __ATOMIC_RELAXED, __HIP_MEMORY_SCOPE_AGENT); }
; #define XB_SPIN(cond, bar) do { unsigned _sp = 0; while (cond) { __builtin_amdgcn_s_sleep(1); \
;     if ((++_sp & 255u) == 0u) { if (xb_ld(&(bar)[XB_TMO])) break; if (_sp > XB_SPIN_CAP) { atomicAdd(&(bar)[XB_TMO], 1u); break; } } } } while (0)
; __device__ __forceinline__ void xcd_barrier(const XcdBarrier& b) {
;     ...
;         const unsigned old = xb_add(&bar[XB_XSUB(b.x)], 1u);
;         const unsigned gen = old / nloc;
;         if (old + 1u == (gen + 1u) * nloc) {
;             __builtin_amdgcn_fence(__ATOMIC_RELEASE, "agent");
;             asm volatile("s_waitcnt vmcnt(0)" ::: "memory");
;             const unsigned og = xb_add(&bar[XB_TOP], 1u);
;             const unsigned tg = og / nx;
;             if (og + 1u == (tg + 1u) * nx) xb_add(&bar[XB_TOPGEN], 1u);
;             else XB_SPIN(xb_ld(&bar[XB_TOPGEN]) == tg, bar);
.LBB0_1718:
	v_readlane_b32 s6, v252, 44
	s_lshl_b32 s6, s6, 2
	s_add_u32 s6, s4, s6
	s_addc_u32 s7, s5, 0
	v_mov_b32_e32 v1, 0x1000
	v_cvt_f32_u32_e32 v3, v4
	buffer_inv sc1
	global_atomic_add v1, v1, v181, s[6:7] offset:1024 sc0
	v_sub_u32_e32 v5, 0, v4
	v_rcp_iflag_f32_e32 v3, v3
	s_nop 0
	v_mul_f32_e32 v3, 0x4f7ffffe, v3
	v_cvt_u32_f32_e32 v3, v3
	v_mul_lo_u32 v5, v5, v3
	v_mul_hi_u32 v5, v3, v5
	v_add_u32_e32 v3, v3, v5
	s_waitcnt vmcnt(0)
	v_mul_hi_u32 v3, v1, v3
	v_mul_lo_u32 v5, v3, v4
	v_sub_u32_e32 v5, v1, v5
	v_add_u32_e32 v6, 1, v3
	v_cmp_ge_u32_e32 vcc, v5, v4
	v_add_u32_e32 v1, 1, v1
	s_nop 0
	v_cndmask_b32_e32 v3, v3, v6, vcc
	v_sub_u32_e32 v6, v5, v4
	v_cndmask_b32_e32 v5, v5, v6, vcc
	v_add_u32_e32 v6, 1, v3
	v_cmp_ge_u32_e32 vcc, v5, v4
	s_nop 1
	v_cndmask_b32_e32 v3, v3, v6, vcc
	v_mul_lo_u32 v5, v4, v3
	v_add_u32_e32 v4, v5, v4
	v_cmp_ne_u32_e32 vcc, v1, v4
	s_and_saveexec_b64 s[8:9], vcc
	s_xor_b64 s[8:9], exec, s[8:9]
	s_cbranch_execz .LBB0_1732
	v_mov_b32_e32 v1, 0x2000
	global_load_dword v1, v1, s[6:7] offset:1024 sc1
	s_add_u32 s14, s6, 0x2400
	s_addc_u32 s15, s7, 0
	s_waitcnt vmcnt(0)
	v_cmp_eq_u32_e32 vcc, v1, v3
	s_and_saveexec_b64 s[10:11], vcc
	s_cbranch_execz .LBB0_1731
	s_mov_b32 s26, 1
	s_mov_b64 s[16:17], 0
	s_branch .LBB0_1722

; __device__ __forceinline__ unsigned xb_ld(unsigned* p)              { return __hip_atomic_load(p, __ATOMIC_RELAXED, __HIP_MEMORY_SCOPE_AGENT); }
; #define XB_SPIN(cond, bar) do { unsigned _sp = 0; while (cond) { __builtin_amdgcn_s_sleep(1); \
;     if ((++_sp & 255u) == 0u) { if (xb_ld(&(bar)[XB_TMO])) break; if (_sp > XB_SPIN_CAP) { atomicAdd(&(bar)[XB_TMO], 1u); break; } } } } while (0)
; __device__ __forceinline__ void xcd_barrier(const XcdBarrier& b) {
;     ...
;             XB_SPIN(xb_ld(&bar[XB_XGEN(b.x)]) == gen, bar);
;             __builtin_amdgcn_fence(__ATOMIC_ACQUIRE, "agent");
;             asm volatile("s_waitcnt vmcnt(0)" ::: "memory");
.LBB0_1731:
	s_or_b64 exec, exec, s[10:11]
	s_waitcnt vmcnt(0) lgkmcnt(0)
	s_waitcnt vmcnt(0)
